# baseline (speedup 1.0000x reference)
_Z15k_scatter_gemm1PKiS0_PiPjPyPKfPK6__halfS5_S5_PS6_PfSA_:
	s_cmpk_gt_u32 s2, 0x186
	s_mov_b64 s[4:5], -1
	s_cbranch_scc0 .LBB1_22
	s_load_dwordx2 s[26:27], s[0:1], 0x28
	s_load_dwordx2 s[10:11], s[0:1], 0x30
	s_load_dwordx4 s[28:31], s[0:1], 0x38
	v_lshlrev_b32_e32 v92, 4, v0
	v_add_u32_e32 v93, 0x1000, v92
	v_add_u32_e32 v94, 0x2000, v92
	v_add_u32_e32 v95, 0x3000, v92
	v_add_u32_e32 v96, 0x4000, v92
	v_add_u32_e32 v97, 0x5000, v92
	v_add_u32_e32 v98, 0x6000, v92
	v_add_u32_e32 v99, 0x7000, v92
	v_add_u32_e32 v100, 0x8000, v92
	v_lshlrev_b32_e32 v101, 2, v0
	s_movk_i32 s3, 0x80
	v_cmp_gt_u32_e64 s[8:9], s3, v0
	s_waitcnt lgkmcnt(0)
	global_load_dwordx4 v[104:107], v92, s[10:11]
	global_load_dwordx4 v[108:111], v93, s[10:11]
	global_load_dwordx4 v[112:115], v94, s[10:11]
	global_load_dwordx4 v[116:119], v95, s[10:11]
	global_load_dwordx4 v[120:123], v96, s[10:11]
	global_load_dwordx4 v[124:127], v97, s[10:11]
	global_load_dwordx4 v[128:131], v98, s[10:11]
	global_load_dwordx4 v[132:135], v99, s[10:11]
	s_and_saveexec_b64 s[4:5], s[8:9]
	global_load_dwordx4 v[136:139], v100, s[10:11]
	global_load_dword v140, v101, s[28:29]
	global_load_dword v141, v101, s[30:31]
	s_mov_b64 exec, s[4:5]
	s_lshl_b32 s3, s2, 2
	v_lshrrev_b32_e32 v14, 6, v0
	s_add_i32 s4, s3, 0xfffff9e4
	v_or_b32_e32 v2, s4, v14
	s_movk_i32 s4, 3016
	v_cmp_gt_i32_e32 vcc, s4, v2
	v_and_b32_e32 v1, 15, v0
	v_and_b32_e32 v66, 48, v0
	v_mov_b32_e32 v67, 0
	s_and_saveexec_b64 s[6:7], vcc
	s_cbranch_execz .Lg1_noval
	v_lshl_or_b32 v2, v2, 4, v1
	v_ashrrev_i32_e32 v3, 31, v2
	v_lshlrev_b64 v[2:3], 9, v[2:3]
	v_lshl_add_u64 v[2:3], s[26:27], 0, v[2:3]
	v_lshl_add_u64 v[16:17], v[2:3], 0, v[66:67]
	global_load_dwordx4 v[38:41], v[16:17], off offset:448
	global_load_dwordx4 v[34:37], v[16:17], off offset:384
	global_load_dwordx4 v[46:49], v[16:17], off offset:320
	global_load_dwordx4 v[42:45], v[16:17], off offset:256
	global_load_dwordx4 v[6:9], v[16:17], off offset:192
	global_load_dwordx4 v[18:21], v[16:17], off offset:128
	global_load_dwordx4 v[2:5], v[16:17], off offset:64
	global_load_dwordx4 v[10:13], v[16:17], off
	s_mov_b64 exec, s[6:7]
	s_waitcnt vmcnt(8)
	s_branch .Lg1_stage

.Lg1_stage:
	ds_write_b128 v92, v[104:107]
	ds_write_b128 v92, v[108:111] offset:4096
	ds_write_b128 v92, v[112:115] offset:8192
	ds_write_b128 v92, v[116:119] offset:12288
	ds_write_b128 v92, v[120:123] offset:16384
	ds_write_b128 v92, v[124:127] offset:20480
	ds_write_b128 v92, v[128:131] offset:24576
	ds_write_b128 v92, v[132:135] offset:28672
	s_and_saveexec_b64 s[4:5], s[8:9]
	ds_write_b128 v92, v[136:139] offset:32768
	ds_write2st64_b32 v101, v140, v141 offset0:204 offset1:206
	s_mov_b64 exec, s[4:5]
	s_waitcnt lgkmcnt(0)
	s_barrier
	s_and_saveexec_b64 s[6:7], vcc
	s_cbranch_execz .LBB1_21
	s_load_dwordx2 s[8:9], s[0:1], 0x58
	s_load_dwordx2 s[10:11], s[0:1], 0x48
	v_and_b32_e32 v15, 63, v0
	v_lshl_add_u64 v[68:69], s[26:27], 0, v[66:67]
	s_movk_i32 s4, 0x1100
	v_cmp_gt_u32_e32 vcc, 16, v15
	v_mul_u32_u24_e32 v15, 0x110, v1
	v_mul_u32_u24_e32 v17, 0x1100, v14
	v_mad_u32_u24 v22, v14, s4, v15
	v_lshlrev_b32_e32 v16, 4, v1
	v_add_u32_e32 v25, s3, v14
	v_lshlrev_b32_e32 v14, 4, v14
	v_bfe_u32 v80, v0, 4, 2
	v_or_b32_e32 v24, v17, v16
	v_mov_b32_e32 v17, v67
	v_lshl_or_b32 v82, s2, 6, v14
	v_mbcnt_lo_u32_b32 v14, -1, 0
	s_waitcnt lgkmcnt(0)
	v_lshl_add_u64 v[70:71], s[10:11], 0, v[16:17]
	v_or_b32_e32 v17, 4, v80
	v_mbcnt_hi_u32_b32 v84, -1, v14
	v_lshlrev_b32_e32 v23, 3, v80
	v_mul_u32_u24_e32 v16, 0x110, v80
	v_mul_u32_u24_e32 v17, 0x110, v17
	v_and_b32_e32 v14, 64, v84
	v_subrev_u32_e32 v67, 56, v25
	v_or_b32_e32 v81, 0xffff9e40, v1
	s_mov_b64 s[10:11], 0
	s_movk_i32 s3, 1508
	v_add_u32_e32 v83, v66, v15
	v_xor_b32_e32 v85, 16, v84
	v_add_u32_e32 v86, 64, v14
	v_xor_b32_e32 v87, 32, v84
	v_add_u32_e32 v88, v22, v23
	v_add_u32_e32 v89, v24, v16
	v_add_u32_e32 v90, v24, v17
	s_movk_i32 s12, 1507
	s_waitcnt vmcnt(0)
	s_branch .LBB1_19

_Z12k_fine_gemm1PKjPKyPKiPiS5_S5_S5_PKfPK6__halfS7_S7_PS8_PfSC_:
	s_cmpk_gt_u32 s2, 0x186
	s_mov_b64 s[4:5], -1
	s_cbranch_scc0 .LBB2_22
	s_load_dwordx2 s[26:27], s[0:1], 0x38
	s_load_dwordx2 s[10:11], s[0:1], 0x40
	s_load_dwordx4 s[28:31], s[0:1], 0x48
	v_lshlrev_b32_e32 v92, 4, v0
	v_add_u32_e32 v93, 0x1000, v92
	v_add_u32_e32 v94, 0x2000, v92
	v_add_u32_e32 v95, 0x3000, v92
	v_add_u32_e32 v96, 0x4000, v92
	v_add_u32_e32 v97, 0x5000, v92
	v_add_u32_e32 v98, 0x6000, v92
	v_add_u32_e32 v99, 0x7000, v92
	v_add_u32_e32 v100, 0x8000, v92
	v_lshlrev_b32_e32 v101, 2, v0
	s_movk_i32 s3, 0x80
	v_cmp_gt_u32_e64 s[8:9], s3, v0
	s_waitcnt lgkmcnt(0)
	global_load_dwordx4 v[104:107], v92, s[10:11]
	global_load_dwordx4 v[108:111], v93, s[10:11]
	global_load_dwordx4 v[112:115], v94, s[10:11]
	global_load_dwordx4 v[116:119], v95, s[10:11]
	global_load_dwordx4 v[120:123], v96, s[10:11]
	global_load_dwordx4 v[124:127], v97, s[10:11]
	global_load_dwordx4 v[128:131], v98, s[10:11]
	global_load_dwordx4 v[132:135], v99, s[10:11]
	s_and_saveexec_b64 s[4:5], s[8:9]
	global_load_dwordx4 v[136:139], v100, s[10:11]
	global_load_dword v140, v101, s[28:29]
	global_load_dword v141, v101, s[30:31]
	s_mov_b64 exec, s[4:5]
	s_lshl_b32 s3, s2, 2
	v_lshrrev_b32_e32 v14, 6, v0
	s_addk_i32 s3, 1452
	v_add_u32_e32 v1, s3, v14
	s_movk_i32 s3, 0x186a
	v_cmp_gt_i32_e32 vcc, s3, v1
	v_and_b32_e32 v80, 15, v0
	v_and_b32_e32 v66, 48, v0
	v_mov_b32_e32 v67, 0
	s_and_saveexec_b64 s[6:7], vcc
	s_cbranch_execz .Lg2_noval
	v_lshl_or_b32 v2, v1, 4, v80
	v_ashrrev_i32_e32 v3, 31, v2
	v_lshlrev_b64 v[2:3], 9, v[2:3]
	v_lshl_add_u64 v[2:3], s[26:27], 0, v[2:3]
	v_lshl_add_u64 v[16:17], v[2:3], 0, v[66:67]
	global_load_dwordx4 v[38:41], v[16:17], off offset:448
	global_load_dwordx4 v[34:37], v[16:17], off offset:384
	global_load_dwordx4 v[26:29], v[16:17], off offset:320
	global_load_dwordx4 v[30:33], v[16:17], off offset:256
	global_load_dwordx4 v[6:9], v[16:17], off offset:192
	global_load_dwordx4 v[18:21], v[16:17], off offset:128
	global_load_dwordx4 v[2:5], v[16:17], off offset:64
	global_load_dwordx4 v[10:13], v[16:17], off
	s_mov_b64 exec, s[6:7]
	s_waitcnt vmcnt(8)
	s_branch .Lg2_stage

.Lg2_stage:
	ds_write_b128 v92, v[104:107]
	ds_write_b128 v92, v[108:111] offset:4096
	ds_write_b128 v92, v[112:115] offset:8192
	ds_write_b128 v92, v[116:119] offset:12288
	ds_write_b128 v92, v[120:123] offset:16384
	ds_write_b128 v92, v[124:127] offset:20480
	ds_write_b128 v92, v[128:131] offset:24576
	ds_write_b128 v92, v[132:135] offset:28672
	s_and_saveexec_b64 s[4:5], s[8:9]
	ds_write_b128 v92, v[136:139] offset:32768
	ds_write2st64_b32 v101, v140, v141 offset0:204 offset1:206
	s_mov_b64 exec, s[4:5]
	s_waitcnt lgkmcnt(0)
	s_barrier
	s_and_saveexec_b64 s[6:7], vcc
	s_cbranch_execz .LBB2_21
	s_load_dwordx2 s[8:9], s[0:1], 0x68
	s_load_dwordx2 s[10:11], s[0:1], 0x58
	v_and_b32_e32 v15, 63, v0
	s_movk_i32 s3, 0x1100
	v_cmp_gt_u32_e32 vcc, 16, v15
	v_mul_u32_u24_e32 v15, 0x110, v80
	v_mul_u32_u24_e32 v17, 0x1100, v14
	v_mad_u32_u24 v22, v14, s3, v15
	v_lshlrev_b32_e32 v16, 4, v80
	v_lshlrev_b32_e32 v14, 4, v14
	v_bfe_u32 v81, v0, 4, 2
	v_or_b32_e32 v24, v17, v16
	v_mov_b32_e32 v17, v67
	v_lshl_or_b32 v82, s2, 6, v14
	v_mbcnt_lo_u32_b32 v14, -1, 0
	s_waitcnt lgkmcnt(0)
	v_lshl_add_u64 v[70:71], s[10:11], 0, v[16:17]
	v_or_b32_e32 v17, 4, v81
	v_mbcnt_hi_u32_b32 v84, -1, v14
	v_lshlrev_b32_e32 v23, 3, v81
	v_mul_u32_u24_e32 v16, 0x110, v81
	v_mul_u32_u24_e32 v17, 0x110, v17
	v_and_b32_e32 v14, 64, v84
	v_lshl_add_u64 v[68:69], s[26:27], 0, v[66:67]
	v_or_b32_e32 v67, 0x5ac0, v80
	s_mov_b64 s[10:11], 0
	s_movk_i32 s3, 0x1285
	s_movk_i32 s14, 0x1286
	v_add_u32_e32 v83, v66, v15
	v_xor_b32_e32 v85, 16, v84
	v_add_u32_e32 v86, 64, v14
	v_xor_b32_e32 v87, 32, v84
	v_add_u32_e32 v88, v22, v23
	v_add_u32_e32 v89, v24, v16
	v_add_u32_e32 v90, v24, v17
	s_waitcnt vmcnt(0)
	s_branch .LBB2_19
.LBB2_18:
	s_or_b64 exec, exec, s[12:13]
	v_cvt_pk_f16_f32 v41, v40, v41
	v_cvt_pk_f16_f32 v40, v38, v39
	v_cvt_pk_f16_f32 v38, v62, v63
	v_add_u32_e32 v62, 0x8800, v88
	v_cvt_pk_f16_f32 v37, v36, v37
	v_cvt_pk_f16_f32 v36, v34, v35
	v_cvt_pk_f16_f32 v35, v56, v57
	v_cvt_pk_f16_f32 v34, v54, v55
	ds_write2_b64 v62, v[36:37], v[34:35] offset0:8 offset1:12
	v_cvt_pk_f16_f32 v35, v48, v49
	v_cvt_pk_f16_f32 v34, v46, v47
	v_cvt_pk_f16_f32 v37, v52, v53
	v_cvt_pk_f16_f32 v36, v50, v51
	v_cvt_pk_f16_f32 v39, v64, v65
	ds_write2_b64 v62, v[34:35], v[36:37] offset0:16 offset1:20
	v_cvt_pk_f16_f32 v35, v44, v45
	v_cvt_pk_f16_f32 v34, v42, v43
	v_cvt_pk_f16_f32 v37, v60, v61
	v_cvt_pk_f16_f32 v36, v58, v59
	ds_write2_b64 v62, v[40:41], v[38:39] offset1:4
	ds_write2_b64 v62, v[34:35], v[36:37] offset0:24 offset1:28
	ds_read_b128 v[34:37], v89 offset:34816
	v_add_u32_e32 v44, v81, v82
	v_add_u32_e32 v38, 0x5ac0, v44
	v_ashrrev_i32_e32 v39, 31, v38
	v_lshlrev_b64 v[38:39], 8, v[38:39]
	v_lshl_add_u64 v[42:43], v[70:71], 0, v[38:39]
	ds_read_b128 v[38:41], v90 offset:34816
	s_waitcnt lgkmcnt(1)
	global_store_dwordx4 v[42:43], v[34:37], off
	s_and_b64 s[4:5], exec, s[4:5]
	s_or_b64 s[10:11], s[4:5], s[10:11]
	v_add_u32_e32 v34, 0x5ac4, v44
	v_ashrrev_i32_e32 v35, 31, v34
	v_lshlrev_b64 v[34:35], 8, v[34:35]
	v_lshl_add_u64 v[34:35], v[70:71], 0, v[34:35]
	s_waitcnt lgkmcnt(0)
	global_store_dwordx4 v[34:35], v[38:41], off
	ds_read_b128 v[34:37], v90 offset:35904
	v_add_u32_e32 v82, 0x5e40, v82
	v_add_u32_e32 v38, 0x5ac8, v44
	v_ashrrev_i32_e32 v39, 31, v38
	v_lshlrev_b64 v[38:39], 8, v[38:39]
	v_lshl_add_u64 v[42:43], v[70:71], 0, v[38:39]
	ds_read_b128 v[38:41], v90 offset:36992
	s_waitcnt lgkmcnt(1)
	global_store_dwordx4 v[42:43], v[34:37], off
	s_nop 1
	v_add_u32_e32 v34, 0x5acc, v44
	v_ashrrev_i32_e32 v35, 31, v34
	v_lshlrev_b64 v[34:35], 8, v[34:35]
	v_lshl_add_u64 v[34:35], v[70:71], 0, v[34:35]
	s_waitcnt lgkmcnt(0)
	global_store_dwordx4 v[34:35], v[38:41], off
	s_waitcnt vmcnt(5)
	v_mov_b64_e32 v[36:37], v[32:33]
	v_mov_b64_e32 v[34:35], v[30:31]
	v_mov_b64_e32 v[32:33], v[24:25]
	v_mov_b64_e32 v[30:31], v[22:23]
	s_waitcnt vmcnt(4)
	v_mov_b64_e32 v[40:41], v[28:29]
	v_mov_b64_e32 v[38:39], v[26:27]
	v_mov_b64_e32 v[28:29], v[16:17]
	v_mov_b64_e32 v[26:27], v[14:15]
	s_andn2_b64 exec, exec, s[10:11]
	s_cbranch_execz .LBB2_21
